# v15 with the norm2 rows strided by wave count (any grid size) instead of contiguous blocks
# speedup vs baseline: 1.0008x; 1.0008x over previous
.LBB0_1393:
	s_andn2_b64 vcc, exec, s[0:1]
	s_cbranch_vccnz .LBB0_1456
	s_waitcnt vmcnt(0) lgkmcnt(0)
	s_barrier
	s_load_dwordx2 s[34:35], s[76:77], 0x130
	s_load_dwordx2 s[36:37], s[76:77], 0x140
	s_load_dwordx2 s[38:39], s[76:77], 0x1c0
	s_load_dwordx2 s[40:41], s[76:77], 0x38
	s_load_dwordx2 s[42:43], s[76:77], 0x120
	s_load_dwordx2 s[44:45], s[76:77], 0xb0
	v_readlane_b32 s9, v254, 0
	v_and_b32_e32 v2, 63, v0
	v_lshrrev_b32_e32 v8, 6, v0
	s_nop 0
	v_readfirstlane_b32 s29, v8
	s_waitcnt lgkmcnt(0)
	s_lshl_b32 s0, s28, 16
	s_add_u32 s44, s44, s0
	s_addc_u32 s45, s45, 0
	s_lshl_b32 s0, s28, 12
	s_add_u32 s40, s40, s0
	s_addc_u32 s41, s41, 0
	s_mul_i32 s0, s28, 0x12000
	s_add_u32 s42, s42, s0
	s_addc_u32 s43, s43, 0
	v_lshlrev_b32_e32 v9, 4, v0
	v_lshrrev_b32_e32 v10, 6, v0
	v_mul_u32_u24_e32 v10, 0x410, v10
	v_bfe_u32 v11, v0, 2, 4
	v_lshl_add_u32 v10, v11, 6, v10
	v_and_b32_e32 v11, 3, v0
	v_lshl_add_u32 v10, v11, 4, v10
	s_mov_b64 s[14:15], s[44:45]
	global_load_dwordx4 v[144:147], v9, s[14:15]
	s_add_u32 s14, s14, 0x2000
	s_addc_u32 s15, s15, 0
	global_load_dwordx4 v[148:151], v9, s[14:15]
	s_add_u32 s14, s14, 0x2000
	s_addc_u32 s15, s15, 0
	global_load_dwordx4 v[152:155], v9, s[14:15]
	s_add_u32 s14, s14, 0x2000
	s_addc_u32 s15, s15, 0
	global_load_dwordx4 v[156:159], v9, s[14:15]
	s_add_u32 s14, s14, 0x2000
	s_addc_u32 s15, s15, 0
	global_load_dwordx4 v[160:163], v9, s[14:15]
	s_add_u32 s14, s14, 0x2000
	s_addc_u32 s15, s15, 0
	global_load_dwordx4 v[164:167], v9, s[14:15]
	s_add_u32 s14, s14, 0x2000
	s_addc_u32 s15, s15, 0
	global_load_dwordx4 v[168:171], v9, s[14:15]
	s_add_u32 s14, s14, 0x2000
	s_addc_u32 s15, s15, 0
	global_load_dwordx4 v[172:175], v9, s[14:15]
	s_waitcnt vmcnt(7)
	ds_write_b128 v10, v[144:147] offset:64
	s_waitcnt vmcnt(6)
	ds_write_b128 v10, v[148:151] offset:8384
	s_waitcnt vmcnt(5)
	ds_write_b128 v10, v[152:155] offset:16704
	s_waitcnt vmcnt(4)
	ds_write_b128 v10, v[156:159] offset:25024
	s_waitcnt vmcnt(3)
	ds_write_b128 v10, v[160:163] offset:33344
	s_waitcnt vmcnt(2)
	ds_write_b128 v10, v[164:167] offset:41664
	s_waitcnt vmcnt(1)
	ds_write_b128 v10, v[168:171] offset:49984
	s_waitcnt vmcnt(0)
	ds_write_b128 v10, v[172:175] offset:58304
	v_lshlrev_b32_e32 v3, 6, v2
	v_lshlrev_b32_e32 v4, 5, v2
	v_mul_u32_u24_e32 v7, 0x410, v2
	v_add_u32_e32 v7, 64, v7
	v_and_b32_e32 v9, 1, v2
	v_lshlrev_b32_e32 v9, 3, v9
	v_and_b32_e32 v10, 2, v2
	v_lshl_or_b32 v9, v10, 1, v9
	v_and_b32_e32 v10, 4, v2
	v_lshrrev_b32_e32 v10, 1, v10
	v_or_b32_e32 v9, v9, v10
	v_bfe_u32 v10, v2, 3, 1
	v_or_b32_e32 v9, v9, v10
	v_lshlrev_b32_e32 v5, 15, v9
	v_lshlrev_b32_e32 v6, 10, v9
	s_mov_b32 s58, 0xaaaaaaaa
	s_mov_b32 s59, 0xaaaaaaaa
	s_mov_b32 s60, 0xcccccccc
	s_mov_b32 s61, 0xcccccccc
	s_mov_b32 s62, 0xf0f0f0f0
	s_mov_b32 s63, 0xf0f0f0f0
	s_mov_b32 s64, 0xff00ff00
	s_mov_b32 s65, 0xff00ff00
	s_mov_b32 s66, 0xffff
	s_mov_b32 s67, 0
	v_readlane_b32 s14, v254, 3
	v_readlane_b32 s15, v254, 4
	s_lshl_b32 s9, s9, 3
	s_add_i32 s46, s9, s29
	s_load_dword s49, s[14:15], 0x0
	s_cmp_eq_u32 s28, 3
	s_movk_i32 s0, 0x4000
	s_cselect_b32 s47, s0, 0x4200
	s_mov_b32 s48, -1
	s_waitcnt lgkmcnt(0)
	s_lshl_b32 s49, s49, 3
	s_lshl_b32 s68, s49, 12
	s_lshl_b32 s0, s46, 12
	s_add_u32 s50, s34, s0
	s_addc_u32 s51, s35, 0
	global_load_dwordx4 v[16:19], v3, s[50:51] offset:0
	global_load_dwordx4 v[20:23], v3, s[50:51] offset:16
	global_load_dwordx4 v[24:27], v3, s[50:51] offset:32
	global_load_dwordx4 v[28:31], v3, s[50:51] offset:48
	s_waitcnt lgkmcnt(0)
	s_barrier

.Ln2_wa_ok:
	s_add_i32 s0, s46, s49
	s_cmp_lt_u32 s0, s47
	s_cbranch_scc0 .Ln2_last
	s_add_u32 s52, s50, s68
	s_addc_u32 s53, s51, 0
	global_load_dwordx4 v[32:35], v3, s[52:53] offset:0
	global_load_dwordx4 v[36:39], v3, s[52:53] offset:16
	global_load_dwordx4 v[40:43], v3, s[52:53] offset:32
	global_load_dwordx4 v[44:47], v3, s[52:53] offset:48
	s_waitcnt vmcnt(4)
	s_branch .Ln2_go

.Ln2_affdone:
	s_mov_b64 exec, -1
	s_add_i32 s46, s46, s49
	s_cmp_lt_u32 s46, s47
	s_cbranch_scc0 .Ln2_done
	s_mov_b64 s[50:51], s[52:53]
	s_waitcnt vmcnt(3)
	v_mov_b32_e32 v16, v32
	v_mov_b32_e32 v17, v33
	v_mov_b32_e32 v18, v34
	v_mov_b32_e32 v19, v35
	v_mov_b32_e32 v20, v36
	v_mov_b32_e32 v21, v37
	v_mov_b32_e32 v22, v38
	v_mov_b32_e32 v23, v39
	v_mov_b32_e32 v24, v40
	v_mov_b32_e32 v25, v41
	v_mov_b32_e32 v26, v42
	v_mov_b32_e32 v27, v43
	v_mov_b32_e32 v28, v44
	v_mov_b32_e32 v29, v45
	v_mov_b32_e32 v30, v46
	v_mov_b32_e32 v31, v47
	s_branch .Ln2_row
